# P2 GLA prep: next unit's gate-activation and q/k loads prefetched during the current unit's gate maths (copied into place at the loop top)
# baseline (speedup 1.0000x reference)
; #define REP(k) for (int rep_ = 0; rep_ < ((PROBE_DUP) == (k) ? 2 : 1); ++rep_)
; __device__ __forceinline__ unsigned pk2(float lo, float hi) { return f2bf(lo) | (f2bf(hi) << 16); }
; __device__ __forceinline__ void gla_prep_unit(Frame& F, int unit) {
;     ...
;           const int c = 16 * mi + fr, j0 = 16 * ni + 4 * fq; float v[4];
; #pragma unroll
;           for (int i = 0; i < 4; ++i) v[i] = (j0 + i <= c) ? acc[i] : 0.f;
;           u32x2 w; w.x = pk2(v[0], v[1]); w.y = pk2(v[2], v[3]); *(u32x2*)(AM + c * 64 + j0) = w; } }
;     __syncthreads();
; __global__ void __launch_bounds__(NTHREADS, 2) hymba_fwd(Args args) {
;     ...
;         REP(20) for (int u = F.bid; u < 2048; u += F.G) gla_prep_unit(F, u);
.LBB0_263:
	s_nop 6
	v_cndmask_b32_e64 v2, v2, 0, s[20:21]
	v_bfe_u32 v6, v2, 16, 1
	v_cndmask_b32_e64 v3, 0, v3, s[22:23]
	v_add3_u32 v2, v2, v6, s55
	v_bfe_u32 v6, v3, 16, 1
	v_lshrrev_b32_e32 v2, 16, v2
	v_add3_u32 v3, v3, v6, s55
	v_and_or_b32 v2, v3, s45, v2
	v_cndmask_b32_e64 v3, v4, 0, s[24:25]
	v_bfe_u32 v4, v3, 16, 1
	v_add3_u32 v3, v3, v4, s55
	v_cndmask_b32_e64 v4, v5, 0, s[26:27]
	v_bfe_u32 v5, v4, 16, 1
	v_readlane_b32 s60, v254, 25
	v_lshrrev_b32_e32 v3, 16, v3
	v_add3_u32 v4, v4, v5, s55
	v_readlane_b32 s66, v254, 31
	v_readlane_b32 s67, v254, 32
	s_add_i32 s57, s57, s90
	s_add_i32 s3, s3, s42
	v_and_or_b32 v3, v4, s45, v3
	v_readlane_b32 s61, v254, 26
	v_readlane_b32 s62, v254, 27
	v_readlane_b32 s63, v254, 28
	v_readlane_b32 s64, v254, 29
	v_readlane_b32 s65, v254, 30
	v_lshl_add_u64 v[4:5], s[66:67], 0, v[20:21]
	v_lshl_add_u64 v[18:19], v[18:19], 0, s[36:37]
	v_lshl_add_u64 v[20:21], v[20:21], 0, s[38:39]
	v_lshl_add_u64 v[22:23], v[22:23], 0, s[38:39]
	v_lshl_add_u64 v[26:27], v[26:27], 0, s[40:41]
	v_lshl_add_u64 v[28:29], v[28:29], 0, s[40:41]
	v_lshl_add_u64 v[30:31], v[30:31], 0, s[40:41]
	v_lshl_add_u64 v[32:33], v[32:33], 0, s[40:41]
	v_lshl_add_u64 v[34:35], v[34:35], 0, s[40:41]
	v_lshl_add_u64 v[36:37], v[36:37], 0, s[40:41]
	v_lshl_add_u64 v[38:39], v[38:39], 0, s[40:41]
	v_lshl_add_u64 v[40:41], v[40:41], 0, s[40:41]
	v_lshl_add_u64 v[42:43], v[42:43], 0, s[40:41]
	v_lshl_add_u64 v[44:45], v[44:45], 0, s[40:41]
	v_lshl_add_u64 v[46:47], v[46:47], 0, s[40:41]
	v_lshl_add_u64 v[48:49], v[48:49], 0, s[40:41]
	v_lshl_add_u64 v[50:51], v[50:51], 0, s[40:41]
	v_lshl_add_u64 v[52:53], v[52:53], 0, s[40:41]
	v_lshl_add_u64 v[54:55], v[54:55], 0, s[40:41]
	v_lshl_add_u64 v[56:57], v[56:57], 0, s[40:41]
	s_cmpk_gt_i32 s57, 0x7ff
	v_lshl_add_u64 v[24:25], v[24:25], 0, s[40:41]
	global_store_dwordx2 v[4:5], v[2:3], off
	s_barrier
	s_cbranch_scc1 .LBB0_270
	s_and_b32 s0, s57, 0x380
	v_readlane_b32 s68, v254, 36
	s_waitcnt vmcnt(18)
	v_mov_b32_e32 v89, v197
	v_mov_b32_e32 v90, v198
	v_mov_b32_e32 v91, v199
	v_mov_b32_e32 v92, v200
	v_mov_b32_e32 v93, v201
	v_mov_b32_e32 v94, v202
	v_mov_b32_e32 v95, v203
	v_mov_b32_e32 v96, v204
	v_mov_b32_e32 v97, v205
	v_mov_b32_e32 v98, v206
	v_mov_b32_e32 v99, v207
	v_mov_b32_e32 v100, v208
	v_mov_b32_e32 v101, v209
	v_mov_b32_e32 v102, v210
	v_mov_b32_e32 v103, v211
	v_mov_b32_e32 v104, v212
	v_mov_b32_e32 v105, v213
	v_mov_b32_e32 v106, v214
	v_mov_b32_e32 v107, v215
	v_mov_b32_e32 v108, v216
	v_mov_b32_e32 v109, v217
	v_mov_b32_e32 v110, v218
	v_mov_b32_e32 v111, v219
	v_mov_b32_e32 v112, v220
	v_mov_b32_e32 v113, v221
	v_mov_b32_e32 v114, v222
	v_mov_b32_e32 v115, v223
	v_mov_b32_e32 v116, v224
	v_mov_b32_e32 v117, v225
	v_mov_b32_e32 v118, v226
	v_mov_b32_e32 v119, v227
	v_mov_b32_e32 v120, v228
	v_mov_b32_e32 v193, v196
	s_branch .Lprep_join

; #define LAS __attribute__((address_space(3)))
; __device__ __forceinline__ void gla_prep_unit(Frame& F, int unit) {
;     ...
;     for (int i = 0; i < 16; ++i) { const bf16_t* pr = PROJ + (m0 + cg * 16 + i) * LDP + h * 128 + d; qv[i] = pr[C_GQ]; kv[i] = pr[C_GK]; }
;     { const int c = tid >> 3, r2 = (tid & 7) * 2; const unsigned w = *(const unsigned*)(PROJ + (m0 + c) * LDP + C_GA + r2); gaS[c * 16 + r2] = bflo(w); gaS[c * 16 + r2 + 1] = bfhi(w); }
;     float w2r[16];
; #pragma unroll
;     for (int r = 0; r < 16; ++r) w2r[r] = F.w2[r * 1024 + h * 128 + d];
;     const float bias = F.gb[h * 128 + d];
;     __syncthreads();
;     float bl[16]; float run = 0.f;
; #pragma unroll
;     for (int i = 0; i < 16; ++i) { const int c = cg * 16 + i; float z = bias;
; #pragma unroll
;         for (int r4 = 0; r4 < 4; ++r4) { const f32x4 g4 = *(const LAS f32x4*)(gaS + c * 16 + 4 * r4); z += g4.x * w2r[4 * r4] + g4.y * w2r[4 * r4 + 1] + g4.z * w2r[4 * r4 + 2] + g4.w * w2r[4 * r4 + 3]; }
.Lprep_join:
	v_or_b32_e32 v2, s0, v10
	v_readlane_b32 s69, v254, 37
	v_readlane_b32 s70, v254, 38
	v_readlane_b32 s71, v254, 39
	v_readlane_b32 s72, v254, 40
	v_readlane_b32 s73, v254, 41
	v_readlane_b32 s74, v254, 42
	v_readlane_b32 s75, v254, 43
	v_readlane_b32 s76, v254, 44
	v_readlane_b32 s77, v254, 45
	v_lshlrev_b32_e32 v122, 2, v2
	v_mov_b32_e32 v123, v9
	v_readlane_b32 s78, v254, 46
	v_readlane_b32 s79, v254, 47
	v_readlane_b32 s80, v254, 48
	v_readlane_b32 s81, v254, 49
	v_readlane_b32 s82, v254, 50
	v_readlane_b32 s83, v254, 51
	s_mov_b64 s[68:69], s[76:77]
	v_lshl_add_u64 v[124:125], s[68:69], 0, v[122:123]
	s_movk_i32 s0, 0x2000
	v_add_co_u32_e32 v4, vcc, s0, v124
	s_movk_i32 s0, 0x6000
	s_nop 0
	v_addc_co_u32_e32 v5, vcc, 0, v125, vcc
	v_add_co_u32_e32 v60, vcc, s44, v124
	global_load_dword v2, v122, s[68:69]
	s_nop 0
	v_addc_co_u32_e32 v61, vcc, 0, v125, vcc
	global_load_dword v6, v[4:5], off offset:-4096
	s_nop 0
	global_load_dword v4, v[4:5], off
	s_nop 0
	global_load_dword v58, v[60:61], off offset:-4096
	global_load_dword v3, v[60:61], off
	v_add_co_u32_e32 v60, vcc, s0, v124
	s_mov_b32 s0, 0xa000
	s_nop 0
	v_addc_co_u32_e32 v61, vcc, 0, v125, vcc
	global_load_dword v7, v[60:61], off offset:-4096
	global_load_dword v5, v[60:61], off
	v_add_co_u32_e32 v60, vcc, s46, v124
	s_mov_b64 s[70:71], s[78:79]
	s_nop 0
	v_addc_co_u32_e32 v61, vcc, 0, v125, vcc
	v_add_co_u32_e32 v62, vcc, s0, v124
	global_load_dword v59, v[60:61], off offset:-4096
	s_nop 0
	global_load_dword v60, v[60:61], off
	v_addc_co_u32_e32 v63, vcc, 0, v125, vcc
	v_add_co_u32_e32 v126, vcc, s47, v124
	global_load_dword v64, v[62:63], off offset:-4096
	s_nop 0
	global_load_dword v62, v[62:63], off
	v_addc_co_u32_e32 v127, vcc, 0, v125, vcc
	global_load_dword v66, v[126:127], off offset:-4096
	global_load_dword v61, v[126:127], off
	v_add_co_u32_e32 v126, vcc, s48, v124
	s_mov_b64 s[72:73], s[80:81]
	s_nop 0
	v_addc_co_u32_e32 v127, vcc, 0, v125, vcc
	v_add_co_u32_e32 v124, vcc, s49, v124
	global_load_dword v65, v[126:127], off offset:-4096
	global_load_dword v63, v[126:127], off
	v_addc_co_u32_e32 v125, vcc, 0, v125, vcc
	global_load_dword v67, v[124:125], off
	global_load_dword v121, v122, s[70:71]
	s_waitcnt vmcnt(49)
	v_lshlrev_b32_e32 v194, 16, v193
	v_and_b32_e32 v195, 0xffff0000, v193
	ds_write_b64 v11, v[194:195]
	s_waitcnt lgkmcnt(0)
	s_barrier
	ds_read_b128 v[122:125], v13
	ds_read_b128 v[126:129], v13 offset:16
	ds_read_b128 v[132:135], v13 offset:32
	ds_read_b128 v[136:139], v13 offset:48
	s_mov_b64 s[74:75], s[82:83]
	s_waitcnt lgkmcnt(3)
	v_mov_b32_e32 v140, v122
	s_waitcnt lgkmcnt(2)
	v_mov_b32_e32 v141, v126
	v_mov_b32_e32 v126, v123
	s_waitcnt vmcnt(11)
	v_pk_mul_f32 v[122:123], v[6:7], v[126:127]
	s_nop 0
	v_pk_fma_f32 v[122:123], v[2:3], v[140:141], v[122:123]
	v_mov_b32_e32 v126, v124
	v_mov_b32_e32 v127, v128
	s_waitcnt vmcnt(10)
	v_pk_fma_f32 v[122:123], v[4:5], v[126:127], v[122:123]
	v_mov_b32_e32 v128, v125
	s_waitcnt vmcnt(9)
	v_pk_fma_f32 v[122:123], v[58:59], v[128:129], v[122:123]
	s_waitcnt vmcnt(0)
	s_add_i32 s98, s57, s90
	s_add_i32 s99, s3, s42
	s_cmpk_gt_i32 s98, 0x7ff
	s_cbranch_scc1 .Lprep_nopf
	s_ashr_i32 s58, s98, 10
	s_ashr_i32 s59, s58, 31
	s_and_b32 s0, s98, 0x380
	s_lshl_b64 s[58:59], s[58:59], 13
	s_and_b32 s1, s99, 0x1fc0
	s_or_b32 s1, s58, s1
	s_lshl_b32 s28, s0, 1
	v_or_b32_e32 v232, s1, v12
	v_lshl_add_u64 v[230:231], v[14:15], 0, s[28:29]
	v_mad_u64_u32 v[230:231], s[60:61], v232, s43, v[230:231]
	v_or_b32_e32 v234, s1, v168
	v_mov_b64_e32 v[232:233], s[96:97]
	v_mad_u64_u32 v[232:233], s[60:61], v234, s43, v[232:233]
	v_mad_i32_i24 v233, s59, v87, v233
	v_lshl_add_u64 v[232:233], v[232:233], 0, v[8:9]
	v_add_co_u32_e32 v232, vcc, s44, v232
	v_mad_i32_i24 v231, s59, v87, v231
	s_nop 0
	v_addc_co_u32_e32 v233, vcc, 0, v233, vcc
	global_load_dword v196, v[232:233], off offset:1024
	v_add_co_u32_e32 v234, vcc, s44, v230
	s_mov_b32 s1, 0xd000
	s_nop 0
	v_addc_co_u32_e32 v235, vcc, 0, v231, vcc
	v_add_co_u32_e32 v236, vcc, s46, v230
	global_load_ushort v227, v[234:235], off offset:1536
	s_nop 0
	v_addc_co_u32_e32 v237, vcc, 0, v231, vcc
	global_load_ushort v225, v[236:237], off offset:3072
	v_add_co_u32_e32 v236, vcc, s1, v230
	s_mov_b32 s1, 0x9000
	s_nop 0
	v_addc_co_u32_e32 v237, vcc, 0, v231, vcc
	v_add_co_u32_e32 v238, vcc, s1, v230
	s_mov_b32 s1, 0x11000
	s_nop 0
	v_addc_co_u32_e32 v239, vcc, 0, v231, vcc
	global_load_ushort v226, v[236:237], off offset:512
	global_load_ushort v228, v[230:231], off
	global_load_ushort v222, v[238:239], off offset:1024
	global_load_ushort v223, v[230:231], off offset:2048
	global_load_ushort v219, v[234:235], off offset:3584
	global_load_ushort v220, v[236:237], off offset:2560
	v_add_co_u32_e32 v234, vcc, s1, v230
	s_mov_b32 s1, 0x15000
	s_nop 0
	v_addc_co_u32_e32 v235, vcc, 0, v231, vcc
	global_load_ushort v218, v[234:235], off offset:2048
	v_add_co_u32_e32 v234, vcc, s1, v230
	s_mov_b32 s1, 0x1a000
	s_nop 0
	v_addc_co_u32_e32 v235, vcc, 0, v231, vcc
	global_load_ushort v217, v[234:235], off offset:3584
	v_add_co_u32_e32 v234, vcc, s1, v230
	s_mov_b32 s1, 0x1e000
	s_nop 0
	v_addc_co_u32_e32 v235, vcc, 0, v231, vcc
	v_add_co_u32_e32 v236, vcc, s1, v230
	s_mov_b32 s1, 0x12000
	s_nop 0
	v_addc_co_u32_e32 v237, vcc, 0, v231, vcc
	global_load_ushort v215, v[234:235], off offset:1024
	global_load_ushort v212, v[236:237], off offset:2560
	v_add_co_u32_e32 v236, vcc, s1, v230
	s_mov_b32 s1, 0x16000
	s_nop 0
	v_addc_co_u32_e32 v237, vcc, 0, v231, vcc
	global_load_ushort v208, v[236:237], off
	global_load_ushort v209, v[234:235], off offset:3072
	v_add_co_u32_e32 v234, vcc, s1, v230
; #define LAS __attribute__((address_space(3)))
; __device__ __forceinline__ void gla_prep_unit(Frame& F, int unit) {
;     ...
;     for (int i = 0; i < 16; ++i) { const bf16_t* pr = PROJ + (m0 + cg * 16 + i) * LDP + h * 128 + d; qv[i] = pr[C_GQ]; kv[i] = pr[C_GK]; }
;     { const int c = tid >> 3, r2 = (tid & 7) * 2; const unsigned w = *(const unsigned*)(PROJ + (m0 + c) * LDP + C_GA + r2); gaS[c * 16 + r2] = bflo(w); gaS[c * 16 + r2 + 1] = bfhi(w); }
;     float w2r[16];
; #pragma unroll
;     for (int r = 0; r < 16; ++r) w2r[r] = F.w2[r * 1024 + h * 128 + d];
;     const float bias = F.gb[h * 128 + d];
;     __syncthreads();
;     float bl[16]; float run = 0.f;
; #pragma unroll
;     for (int i = 0; i < 16; ++i) { const int c = cg * 16 + i; float z = bias;
; #pragma unroll
;         for (int r4 = 0; r4 < 4; ++r4) { const f32x4 g4 = *(const LAS f32x4*)(gaS + c * 16 + 4 * r4); z += g4.x * w2r[4 * r4] + g4.y * w2r[4 * r4 + 1] + g4.z * w2r[4 * r4 + 2] + g4.w * w2r[4 * r4 + 3]; }
;         const float ls = fminf(z, 0.f) - __logf(1.0f + __expf(-fabsf(z)));
;         run += ls * (1.f / 16.f); bl[i] = run; }
	s_mov_b32 s1, 0x1f000
	s_nop 0
	v_addc_co_u32_e32 v235, vcc, 0, v231, vcc
	global_load_ushort v210, v[234:235], off offset:1536
	v_add_co_u32_e32 v234, vcc, s1, v230
	s_mov_b32 s1, 0x23000
	s_nop 0
	v_addc_co_u32_e32 v235, vcc, 0, v231, vcc
	global_load_ushort v213, v[234:235], off offset:512
	v_add_co_u32_e32 v234, vcc, s1, v230
	s_mov_b32 s1, 0x27000
	s_nop 0
	v_addc_co_u32_e32 v235, vcc, 0, v231, vcc
	v_add_co_u32_e32 v236, vcc, s1, v230
	s_mov_b32 s1, 0x2b000
	s_nop 0
	v_addc_co_u32_e32 v237, vcc, 0, v231, vcc
	v_add_co_u32_e32 v238, vcc, s1, v230
	s_mov_b32 s1, 0x30000
	s_nop 0
	v_addc_co_u32_e32 v239, vcc, 0, v231, vcc
	global_load_ushort v224, v[234:235], off
	global_load_ushort v221, v[236:237], off offset:1536
	global_load_ushort v216, v[238:239], off offset:3072
	v_add_co_u32_e32 v238, vcc, s1, v230
	s_mov_b32 s1, 0x2c000
	s_nop 0
	v_addc_co_u32_e32 v239, vcc, 0, v231, vcc
	global_load_ushort v214, v[238:239], off offset:512
	global_load_ushort v207, v[234:235], off offset:2048
	v_add_co_u32_e32 v234, vcc, s1, v230
	s_mov_b32 s1, 0x34000
	s_nop 0
	v_addc_co_u32_e32 v235, vcc, 0, v231, vcc
	global_load_ushort v211, v[234:235], off offset:1024
	global_load_ushort v205, v[236:237], off offset:3584
	global_load_ushort v206, v[238:239], off offset:2560
	v_add_co_u32_e32 v234, vcc, s1, v230
	s_mov_b32 s1, 0x38000
	s_nop 0
	v_addc_co_u32_e32 v235, vcc, 0, v231, vcc
	global_load_ushort v204, v[234:235], off offset:2048
	v_add_co_u32_e32 v234, vcc, s1, v230
	s_mov_b32 s1, 0x3d000
	s_nop 0
	v_addc_co_u32_e32 v235, vcc, 0, v231, vcc
	global_load_ushort v203, v[234:235], off offset:3584
	v_add_co_u32_e32 v234, vcc, s1, v230
	s_mov_b32 s1, 0x41000
	s_nop 0
	v_addc_co_u32_e32 v235, vcc, 0, v231, vcc
	v_add_co_u32_e32 v236, vcc, s1, v230
	s_mov_b32 s1, 0x35000
	s_nop 0
	v_addc_co_u32_e32 v237, vcc, 0, v231, vcc
	global_load_ushort v202, v[234:235], off offset:1024
	global_load_ushort v201, v[236:237], off offset:2560
	v_add_co_u32_e32 v236, vcc, s1, v230
	s_mov_b32 s1, 0x39000
	s_nop 0
	v_addc_co_u32_e32 v237, vcc, 0, v231, vcc
	global_load_ushort v199, v[236:237], off
	global_load_ushort v200, v[234:235], off offset:3072
	v_add_co_u32_e32 v234, vcc, s1, v230
	s_mov_b32 s1, 0x42000
	s_nop 0
	v_addc_co_u32_e32 v235, vcc, 0, v231, vcc
	v_add_co_u32_e32 v230, vcc, s1, v230
	s_nop 0
	v_addc_co_u32_e32 v231, vcc, 0, v231, vcc
	global_load_ushort v197, v[234:235], off offset:1536
	global_load_ushort v198, v[230:231], off offset:512
.Lprep_nopf:
	v_add_f32_e32 v122, v121, v122
	v_add_f32_e32 v126, v122, v123
	s_waitcnt lgkmcnt(0)
	v_mov_b32_e32 v123, v136
	v_mov_b32_e32 v136, v133
	v_mov_b32_e32 v122, v132
	v_pk_mul_f32 v[124:125], v[64:65], v[136:137]
	s_nop 0
	v_pk_fma_f32 v[122:123], v[60:61], v[122:123], v[124:125]
	v_mov_b32_e32 v124, v134
	v_mov_b32_e32 v125, v138
	v_pk_fma_f32 v[122:123], v[62:63], v[124:125], v[122:123]
	v_mov_b32_e32 v138, v135
	v_pk_fma_f32 v[122:123], v[66:67], v[138:139], v[122:123]
	s_nop 0
	v_add_f32_e32 v122, v126, v122
	v_add_f32_e32 v122, v122, v123
	v_min_f32_e32 v123, 0, v122
	v_mul_f32_e64 v122, |v122|, s50
	v_exp_f32_e32 v122, v122
	s_nop 0
	v_add_f32_e32 v122, 1.0, v122
	v_cmp_gt_f32_e32 vcc, s51, v122
	s_nop 1
	v_cndmask_b32_e64 v124, 0, 32, vcc
	v_ldexp_f32 v122, v122, v124
	v_log_f32_e32 v122, v122
	s_nop 0
	v_mul_f32_e32 v124, 0x3f317217, v122
	v_fma_f32 v124, v122, s52, -v124
	v_fmac_f32_e32 v124, 0x3377d1cf, v122
	v_fmac_f32_e32 v124, 0x3f317217, v122
	v_cmp_lt_f32_e64 s[0:1], |v122|, s53
	s_nop 1
	v_cndmask_b32_e64 v122, v122, v124, s[0:1]
	v_cndmask_b32_e32 v124, 0, v88, vcc
	v_sub_f32_e32 v122, v122, v124
	ds_read_b128 v[124:127], v13 offset:64
	ds_read_b128 v[132:135], v13 offset:80
	v_sub_f32_e32 v122, v123, v122
	v_fma_f32 v122, v122, s54, 0
	s_waitcnt lgkmcnt(1)
	v_mov_b32_e32 v128, v124
	s_waitcnt lgkmcnt(0)
	v_mov_b32_e32 v129, v132
	v_mov_b32_e32 v132, v125
	v_pk_mul_f32 v[124:125], v[6:7], v[132:133]
	s_nop 0
	v_pk_fma_f32 v[124:125], v[2:3], v[128:129], v[124:125]
	v_mov_b32_e32 v128, v126
	v_mov_b32_e32 v129, v134
	v_pk_fma_f32 v[124:125], v[4:5], v[128:129], v[124:125]
	v_mov_b32_e32 v134, v127
	v_pk_fma_f32 v[124:125], v[58:59], v[134:135], v[124:125]
	s_nop 0
	v_add_f32_e32 v123, v121, v124
	v_add_f32_e32 v123, v123, v125
	ds_read_b128 v[124:127], v13 offset:96
	ds_read_b128 v[132:135], v13 offset:112
	s_waitcnt lgkmcnt(1)
	v_mov_b32_e32 v128, v124
	s_waitcnt lgkmcnt(0)
	v_mov_b32_e32 v129, v132
	v_mov_b32_e32 v132, v125
	v_pk_mul_f32 v[124:125], v[64:65], v[132:133]
	s_nop 0
	v_pk_fma_f32 v[124:125], v[60:61], v[128:129], v[124:125]
	v_mov_b32_e32 v128, v126
	v_mov_b32_e32 v129, v134
	v_pk_fma_f32 v[124:125], v[62:63], v[128:129], v[124:125]
	v_mov_b32_e32 v134, v127
	v_pk_fma_f32 v[124:125], v[66:67], v[134:135], v[124:125]
	s_nop 0
	v_add_f32_e32 v123, v123, v124
	v_add_f32_e32 v123, v123, v125
	v_min_f32_e32 v124, 0, v123
	v_mul_f32_e64 v123, |v123|, s50
	v_exp_f32_e32 v123, v123
	s_nop 0
	v_add_f32_e32 v123, 1.0, v123
	v_cmp_gt_f32_e32 vcc, s51, v123
	s_nop 1
	v_cndmask_b32_e64 v125, 0, 32, vcc
	v_ldexp_f32 v123, v123, v125
	v_log_f32_e32 v123, v123
	s_nop 0
	v_mul_f32_e32 v125, 0x3f317217, v123
	v_fma_f32 v125, v123, s52, -v125
	v_fmac_f32_e32 v125, 0x3377d1cf, v123
	v_fmac_f32_e32 v125, 0x3f317217, v123
	v_cmp_lt_f32_e64 s[0:1], |v123|, s53
	s_nop 1
	v_cndmask_b32_e64 v123, v123, v125, s[0:1]
	v_cndmask_b32_e32 v125, 0, v88, vcc
	v_sub_f32_e32 v123, v123, v125
	v_sub_f32_e32 v123, v124, v123
	ds_read_b128 v[124:127], v13 offset:128
	ds_read_b128 v[132:135], v13 offset:144
	v_fmamk_f32 v123, v123, 0x3d800000, v122
	s_waitcnt lgkmcnt(1)
	v_mov_b32_e32 v128, v124
	s_waitcnt lgkmcnt(0)
; #define LAS __attribute__((address_space(3)))
; __device__ __forceinline__ void gla_prep_unit(Frame& F, int unit) {
;     ...
;     for (int i = 0; i < 16; ++i) { const int c = cg * 16 + i; float z = bias;
; #pragma unroll
;         for (int r4 = 0; r4 < 4; ++r4) { const f32x4 g4 = *(const LAS f32x4*)(gaS + c * 16 + 4 * r4); z += g4.x * w2r[4 * r4] + g4.y * w2r[4 * r4 + 1] + g4.z * w2r[4 * r4 + 2] + g4.w * w2r[4 * r4 + 3]; }
;         const float ls = fminf(z, 0.f) - __logf(1.0f + __expf(-fabsf(z)));
;         run += ls * (1.f / 16.f); bl[i] = run; }
	v_mov_b32_e32 v129, v132
	v_mov_b32_e32 v132, v125
	v_pk_mul_f32 v[124:125], v[6:7], v[132:133]
	s_nop 0
	v_pk_fma_f32 v[124:125], v[2:3], v[128:129], v[124:125]
	v_mov_b32_e32 v128, v126
	v_mov_b32_e32 v129, v134
	v_pk_fma_f32 v[124:125], v[4:5], v[128:129], v[124:125]
	v_mov_b32_e32 v134, v127
	v_pk_fma_f32 v[124:125], v[58:59], v[134:135], v[124:125]
	s_nop 0
	v_add_f32_e32 v124, v121, v124
	v_add_f32_e32 v136, v124, v125
	ds_read_b128 v[124:127], v13 offset:160
	ds_read_b128 v[132:135], v13 offset:176
	s_waitcnt lgkmcnt(1)
	v_mov_b32_e32 v128, v124
	s_waitcnt lgkmcnt(0)
	v_mov_b32_e32 v129, v132
	v_mov_b32_e32 v132, v125
	v_pk_mul_f32 v[124:125], v[64:65], v[132:133]
	s_nop 0
	v_pk_fma_f32 v[124:125], v[60:61], v[128:129], v[124:125]
	v_mov_b32_e32 v128, v126
	v_mov_b32_e32 v129, v134
	v_pk_fma_f32 v[124:125], v[62:63], v[128:129], v[124:125]
	v_mov_b32_e32 v134, v127
	v_pk_fma_f32 v[124:125], v[66:67], v[134:135], v[124:125]
	s_nop 0
	v_add_f32_e32 v124, v136, v124
	v_add_f32_e32 v124, v124, v125
	v_min_f32_e32 v125, 0, v124
	v_mul_f32_e64 v124, |v124|, s50
	v_exp_f32_e32 v124, v124
	s_nop 0
	v_add_f32_e32 v124, 1.0, v124
	v_cmp_gt_f32_e32 vcc, s51, v124
	s_nop 1
	v_cndmask_b32_e64 v126, 0, 32, vcc
	v_ldexp_f32 v124, v124, v126
	v_log_f32_e32 v124, v124
	s_nop 0
	v_mul_f32_e32 v126, 0x3f317217, v124
	v_fma_f32 v126, v124, s52, -v126
	v_fmac_f32_e32 v126, 0x3377d1cf, v124
	v_fmac_f32_e32 v126, 0x3f317217, v124
	v_cmp_lt_f32_e64 s[0:1], |v124|, s53
	s_nop 1
	v_cndmask_b32_e64 v124, v124, v126, s[0:1]
	v_cndmask_b32_e32 v126, 0, v88, vcc
	v_sub_f32_e32 v124, v124, v126
	ds_read_b128 v[126:129], v13 offset:192
	ds_read_b128 v[132:135], v13 offset:208
	v_sub_f32_e32 v124, v125, v124
	v_fmamk_f32 v124, v124, 0x3d800000, v123
	s_waitcnt lgkmcnt(1)
	v_mov_b32_e32 v136, v126
	s_waitcnt lgkmcnt(0)
	v_mov_b32_e32 v137, v132
	v_mov_b32_e32 v132, v127
	v_pk_mul_f32 v[126:127], v[6:7], v[132:133]
	v_mov_b32_e32 v132, v128
	v_pk_fma_f32 v[126:127], v[2:3], v[136:137], v[126:127]
	v_mov_b32_e32 v133, v134
	v_pk_fma_f32 v[126:127], v[4:5], v[132:133], v[126:127]
	v_mov_b32_e32 v134, v129
	v_pk_fma_f32 v[126:127], v[58:59], v[134:135], v[126:127]
	s_nop 0
	v_add_f32_e32 v125, v121, v126
	v_add_f32_e32 v125, v125, v127
	ds_read_b128 v[126:129], v13 offset:224
	ds_read_b128 v[132:135], v13 offset:240
	s_waitcnt lgkmcnt(1)
	v_mov_b32_e32 v136, v126
	s_waitcnt lgkmcnt(0)
	v_mov_b32_e32 v137, v132
	v_mov_b32_e32 v132, v127
	v_pk_mul_f32 v[126:127], v[64:65], v[132:133]
	v_mov_b32_e32 v132, v128
	v_pk_fma_f32 v[126:127], v[60:61], v[136:137], v[126:127]
	v_mov_b32_e32 v133, v134
	v_pk_fma_f32 v[126:127], v[62:63], v[132:133], v[126:127]
	v_mov_b32_e32 v134, v129
	v_pk_fma_f32 v[126:127], v[66:67], v[134:135], v[126:127]
	s_nop 0
	v_add_f32_e32 v125, v125, v126
	v_add_f32_e32 v125, v125, v127
	v_min_f32_e32 v126, 0, v125
	v_mul_f32_e64 v125, |v125|, s50
	v_exp_f32_e32 v125, v125
	s_nop 0
	v_add_f32_e32 v125, 1.0, v125
	v_cmp_gt_f32_e32 vcc, s51, v125
	s_nop 1
	v_cndmask_b32_e64 v127, 0, 32, vcc
	v_ldexp_f32 v125, v125, v127
	v_log_f32_e32 v125, v125
	s_nop 0
	v_mul_f32_e32 v127, 0x3f317217, v125
	v_fma_f32 v127, v125, s52, -v127
	v_fmac_f32_e32 v127, 0x3377d1cf, v125
	v_fmac_f32_e32 v127, 0x3f317217, v125
	v_cmp_lt_f32_e64 s[0:1], |v125|, s53
	s_nop 1
	v_cndmask_b32_e64 v125, v125, v127, s[0:1]
	v_cndmask_b32_e32 v127, 0, v88, vcc
	v_sub_f32_e32 v125, v125, v127
	v_sub_f32_e32 v125, v126, v125
	ds_read_b128 v[126:129], v13 offset:256
	ds_read_b128 v[132:135], v13 offset:272
	v_fmamk_f32 v125, v125, 0x3d800000, v124
	s_waitcnt lgkmcnt(1)
	v_mov_b32_e32 v136, v126
	s_waitcnt lgkmcnt(0)
	v_mov_b32_e32 v137, v132
	v_mov_b32_e32 v132, v127
	v_pk_mul_f32 v[126:127], v[6:7], v[132:133]
	v_mov_b32_e32 v132, v128
	v_pk_fma_f32 v[126:127], v[2:3], v[136:137], v[126:127]
	v_mov_b32_e32 v133, v134
	v_pk_fma_f32 v[126:127], v[4:5], v[132:133], v[126:127]
	v_mov_b32_e32 v134, v129
	v_pk_fma_f32 v[126:127], v[58:59], v[134:135], v[126:127]
	s_nop 0
	v_add_f32_e32 v126, v121, v126
	v_add_f32_e32 v138, v126, v127
	ds_read_b128 v[126:129], v13 offset:288
	ds_read_b128 v[132:135], v13 offset:304
	s_waitcnt lgkmcnt(1)
	v_mov_b32_e32 v136, v126
	s_waitcnt lgkmcnt(0)
	v_mov_b32_e32 v137, v132
	v_mov_b32_e32 v132, v127
	v_pk_mul_f32 v[126:127], v[64:65], v[132:133]
	v_mov_b32_e32 v132, v128
	v_pk_fma_f32 v[126:127], v[60:61], v[136:137], v[126:127]
	v_mov_b32_e32 v133, v134
	v_pk_fma_f32 v[126:127], v[62:63], v[132:133], v[126:127]
	v_mov_b32_e32 v134, v129
	v_pk_fma_f32 v[126:127], v[66:67], v[134:135], v[126:127]
	s_nop 0
	v_add_f32_e32 v126, v138, v126
	v_add_f32_e32 v126, v126, v127
	v_min_f32_e32 v127, 0, v126
	v_mul_f32_e64 v126, |v126|, s50
	v_exp_f32_e32 v126, v126
	ds_read_b128 v[132:135], v13 offset:320
	ds_read_b128 v[136:139], v13 offset:336
	v_add_f32_e32 v126, 1.0, v126
	v_cmp_gt_f32_e32 vcc, s51, v126
	s_waitcnt lgkmcnt(0)
	v_mov_b32_e32 v129, v136
	v_mov_b32_e32 v136, v133
	v_cndmask_b32_e64 v128, 0, 32, vcc
	v_ldexp_f32 v126, v126, v128
	v_log_f32_e32 v126, v126
	s_nop 0
	v_mul_f32_e32 v128, 0x3f317217, v126
	v_fma_f32 v128, v126, s52, -v128
	v_fmac_f32_e32 v128, 0x3377d1cf, v126
	v_fmac_f32_e32 v128, 0x3f317217, v126
	v_cmp_lt_f32_e64 s[0:1], |v126|, s53
	s_nop 1
	v_cndmask_b32_e64 v126, v126, v128, s[0:1]
	v_cndmask_b32_e32 v128, 0, v88, vcc
	v_sub_f32_e32 v126, v126, v128
	v_mov_b32_e32 v128, v132
	v_pk_mul_f32 v[132:133], v[6:7], v[136:137]
	v_sub_f32_e32 v126, v127, v126
	v_pk_fma_f32 v[128:129], v[2:3], v[128:129], v[132:133]
	v_mov_b32_e32 v132, v134
	v_mov_b32_e32 v133, v138
	v_pk_fma_f32 v[128:129], v[4:5], v[132:133], v[128:129]
	v_mov_b32_e32 v138, v135
	v_pk_fma_f32 v[128:129], v[58:59], v[138:139], v[128:129]
	ds_read_b128 v[132:135], v13 offset:352
	ds_read_b128 v[136:139], v13 offset:368
	v_add_f32_e32 v127, v121, v128
	v_add_f32_e32 v127, v127, v129
	v_fmamk_f32 v126, v126, 0x3d800000, v125
	s_waitcnt lgkmcnt(1)
; #define LAS __attribute__((address_space(3)))
; __device__ __forceinline__ void gla_prep_unit(Frame& F, int unit) {
;     ...
;     for (int i = 0; i < 16; ++i) { const int c = cg * 16 + i; float z = bias;
; #pragma unroll
;         for (int r4 = 0; r4 < 4; ++r4) { const f32x4 g4 = *(const LAS f32x4*)(gaS + c * 16 + 4 * r4); z += g4.x * w2r[4 * r4] + g4.y * w2r[4 * r4 + 1] + g4.z * w2r[4 * r4 + 2] + g4.w * w2r[4 * r4 + 3]; }
;         const float ls = fminf(z, 0.f) - __logf(1.0f + __expf(-fabsf(z)));
;         run += ls * (1.f / 16.f); bl[i] = run; }
	v_mov_b32_e32 v128, v132
	s_waitcnt lgkmcnt(0)
	v_mov_b32_e32 v129, v136
	v_mov_b32_e32 v136, v133
	v_pk_mul_f32 v[132:133], v[64:65], v[136:137]
	s_nop 0
	v_pk_fma_f32 v[128:129], v[60:61], v[128:129], v[132:133]
	v_mov_b32_e32 v132, v134
	v_mov_b32_e32 v133, v138
	v_pk_fma_f32 v[128:129], v[62:63], v[132:133], v[128:129]
	v_mov_b32_e32 v138, v135
	v_pk_fma_f32 v[128:129], v[66:67], v[138:139], v[128:129]
	ds_read_b128 v[132:135], v13 offset:384
	ds_read_b128 v[136:139], v13 offset:400
	v_add_f32_e32 v127, v127, v128
	v_add_f32_e32 v127, v127, v129
	v_min_f32_e32 v128, 0, v127
	v_mul_f32_e64 v127, |v127|, s50
	v_exp_f32_e32 v127, v127
	s_nop 0
	v_add_f32_e32 v127, 1.0, v127
	v_cmp_gt_f32_e32 vcc, s51, v127
	s_nop 1
	v_cndmask_b32_e64 v129, 0, 32, vcc
	v_ldexp_f32 v127, v127, v129
	v_log_f32_e32 v127, v127
	s_nop 0
	v_mul_f32_e32 v129, 0x3f317217, v127
	v_fma_f32 v129, v127, s52, -v129
	v_fmac_f32_e32 v129, 0x3377d1cf, v127
	v_fmac_f32_e32 v129, 0x3f317217, v127
	v_cmp_lt_f32_e64 s[0:1], |v127|, s53
	s_nop 1
	v_cndmask_b32_e64 v127, v127, v129, s[0:1]
	v_cndmask_b32_e32 v129, 0, v88, vcc
	v_sub_f32_e32 v127, v127, v129
	s_waitcnt lgkmcnt(0)
	v_mov_b32_e32 v129, v136
	v_mov_b32_e32 v136, v133
	v_sub_f32_e32 v127, v128, v127
	v_mov_b32_e32 v128, v132
	v_pk_mul_f32 v[132:133], v[6:7], v[136:137]
	v_fmamk_f32 v127, v127, 0x3d800000, v126
	v_pk_fma_f32 v[128:129], v[2:3], v[128:129], v[132:133]
	v_mov_b32_e32 v132, v134
	v_mov_b32_e32 v133, v138
	v_pk_fma_f32 v[128:129], v[4:5], v[132:133], v[128:129]
	v_mov_b32_e32 v138, v135
	v_pk_fma_f32 v[128:129], v[58:59], v[138:139], v[128:129]
	ds_read_b128 v[132:135], v13 offset:416
	ds_read_b128 v[136:139], v13 offset:432
	v_add_f32_e32 v128, v121, v128
	v_add_f32_e32 v140, v128, v129
	s_waitcnt lgkmcnt(1)
	v_mov_b32_e32 v128, v132
	s_waitcnt lgkmcnt(0)
	v_mov_b32_e32 v129, v136
	v_mov_b32_e32 v136, v133
	v_pk_mul_f32 v[132:133], v[64:65], v[136:137]
	s_nop 0
	v_pk_fma_f32 v[128:129], v[60:61], v[128:129], v[132:133]
	v_mov_b32_e32 v132, v134
	v_mov_b32_e32 v133, v138
	v_pk_fma_f32 v[128:129], v[62:63], v[132:133], v[128:129]
	v_mov_b32_e32 v138, v135
	v_pk_fma_f32 v[128:129], v[66:67], v[138:139], v[128:129]
	s_nop 0
	v_add_f32_e32 v128, v140, v128
	v_add_f32_e32 v128, v128, v129
	v_min_f32_e32 v129, 0, v128
	v_mul_f32_e64 v128, |v128|, s50
	v_exp_f32_e32 v128, v128
	s_nop 0
	v_add_f32_e32 v128, 1.0, v128
	v_cmp_gt_f32_e32 vcc, s51, v128
	s_nop 1
	v_cndmask_b32_e64 v132, 0, 32, vcc
	v_ldexp_f32 v128, v128, v132
	v_log_f32_e32 v128, v128
	s_nop 0
	v_mul_f32_e32 v132, 0x3f317217, v128
	v_fma_f32 v132, v128, s52, -v132
	v_fmac_f32_e32 v132, 0x3377d1cf, v128
	v_fmac_f32_e32 v132, 0x3f317217, v128
	v_cmp_lt_f32_e64 s[0:1], |v128|, s53
	s_nop 1
	v_cndmask_b32_e64 v128, v128, v132, s[0:1]
	v_cndmask_b32_e32 v132, 0, v88, vcc
	v_sub_f32_e32 v128, v128, v132
	ds_read_b128 v[132:135], v13 offset:448
	ds_read_b128 v[136:139], v13 offset:464
	v_sub_f32_e32 v128, v129, v128
	v_fmamk_f32 v128, v128, 0x3d800000, v127
	s_waitcnt lgkmcnt(1)
	v_mov_b32_e32 v140, v132
	s_waitcnt lgkmcnt(0)
	v_mov_b32_e32 v141, v136
	v_mov_b32_e32 v136, v133
	v_pk_mul_f32 v[132:133], v[6:7], v[136:137]
	v_mov_b32_e32 v136, v134
	v_pk_fma_f32 v[132:133], v[2:3], v[140:141], v[132:133]
	v_mov_b32_e32 v137, v138
	v_pk_fma_f32 v[132:133], v[4:5], v[136:137], v[132:133]
	v_mov_b32_e32 v138, v135
	v_pk_fma_f32 v[132:133], v[58:59], v[138:139], v[132:133]
	s_nop 0
	v_add_f32_e32 v129, v121, v132
	v_add_f32_e32 v129, v129, v133
	ds_read_b128 v[132:135], v13 offset:480
	ds_read_b128 v[136:139], v13 offset:496
	s_waitcnt lgkmcnt(1)
	v_mov_b32_e32 v140, v132
	s_waitcnt lgkmcnt(0)
	v_mov_b32_e32 v141, v136
	v_mov_b32_e32 v136, v133
	v_pk_mul_f32 v[132:133], v[64:65], v[136:137]
	v_mov_b32_e32 v136, v134
	v_pk_fma_f32 v[132:133], v[60:61], v[140:141], v[132:133]
	v_mov_b32_e32 v137, v138
	v_pk_fma_f32 v[132:133], v[62:63], v[136:137], v[132:133]
	v_mov_b32_e32 v138, v135
	v_pk_fma_f32 v[132:133], v[66:67], v[138:139], v[132:133]
	s_nop 0
	v_add_f32_e32 v129, v129, v132
	v_add_f32_e32 v129, v129, v133
	v_min_f32_e32 v132, 0, v129
	v_mul_f32_e64 v129, |v129|, s50
	v_exp_f32_e32 v129, v129
	s_nop 0
	v_add_f32_e32 v129, 1.0, v129
	v_cmp_gt_f32_e32 vcc, s51, v129
	s_nop 1
	v_cndmask_b32_e64 v133, 0, 32, vcc
	v_ldexp_f32 v129, v129, v133
	v_log_f32_e32 v129, v129
	s_nop 0
	v_mul_f32_e32 v133, 0x3f317217, v129
	v_fma_f32 v133, v129, s52, -v133
	v_fmac_f32_e32 v133, 0x3377d1cf, v129
	v_fmac_f32_e32 v133, 0x3f317217, v129
	v_cmp_lt_f32_e64 s[0:1], |v129|, s53
	s_nop 1
	v_cndmask_b32_e64 v129, v129, v133, s[0:1]
	v_cndmask_b32_e32 v133, 0, v88, vcc
	v_sub_f32_e32 v129, v129, v133
	v_sub_f32_e32 v129, v132, v129
	ds_read_b128 v[132:135], v13 offset:512
	ds_read_b128 v[136:139], v13 offset:528
	v_fmamk_f32 v129, v129, 0x3d800000, v128
	s_waitcnt lgkmcnt(1)
	v_mov_b32_e32 v140, v132
	s_waitcnt lgkmcnt(0)
	v_mov_b32_e32 v141, v136
	v_mov_b32_e32 v136, v133
	v_pk_mul_f32 v[132:133], v[6:7], v[136:137]
	v_mov_b32_e32 v136, v134
	v_pk_fma_f32 v[132:133], v[2:3], v[140:141], v[132:133]
	v_mov_b32_e32 v137, v138
	v_pk_fma_f32 v[132:133], v[4:5], v[136:137], v[132:133]
	v_mov_b32_e32 v138, v135
	v_pk_fma_f32 v[132:133], v[58:59], v[138:139], v[132:133]
	s_nop 0
	v_add_f32_e32 v132, v121, v132
	v_add_f32_e32 v142, v132, v133
	ds_read_b128 v[132:135], v13 offset:544
	ds_read_b128 v[136:139], v13 offset:560
	s_waitcnt lgkmcnt(1)
	v_mov_b32_e32 v140, v132
	s_waitcnt lgkmcnt(0)
; #define LAS __attribute__((address_space(3)))
; __device__ __forceinline__ void gla_prep_unit(Frame& F, int unit) {
;     ...
;     for (int i = 0; i < 16; ++i) { const int c = cg * 16 + i; float z = bias;
; #pragma unroll
;         for (int r4 = 0; r4 < 4; ++r4) { const f32x4 g4 = *(const LAS f32x4*)(gaS + c * 16 + 4 * r4); z += g4.x * w2r[4 * r4] + g4.y * w2r[4 * r4 + 1] + g4.z * w2r[4 * r4 + 2] + g4.w * w2r[4 * r4 + 3]; }
;         const float ls = fminf(z, 0.f) - __logf(1.0f + __expf(-fabsf(z)));
;         run += ls * (1.f / 16.f); bl[i] = run; }
	v_mov_b32_e32 v141, v136
	v_mov_b32_e32 v136, v133
	v_pk_mul_f32 v[132:133], v[64:65], v[136:137]
	v_mov_b32_e32 v136, v134
	v_pk_fma_f32 v[132:133], v[60:61], v[140:141], v[132:133]
	v_mov_b32_e32 v137, v138
	v_pk_fma_f32 v[132:133], v[62:63], v[136:137], v[132:133]
	v_mov_b32_e32 v138, v135
	v_pk_fma_f32 v[132:133], v[66:67], v[138:139], v[132:133]
	s_nop 0
	v_add_f32_e32 v132, v142, v132
	v_add_f32_e32 v132, v132, v133
	v_min_f32_e32 v133, 0, v132
	v_mul_f32_e64 v132, |v132|, s50
	v_exp_f32_e32 v132, v132
	s_nop 0
	v_add_f32_e32 v132, 1.0, v132
	v_cmp_gt_f32_e32 vcc, s51, v132
	s_nop 1
	v_cndmask_b32_e64 v134, 0, 32, vcc
	v_ldexp_f32 v132, v132, v134
	v_log_f32_e32 v132, v132
	s_nop 0
	v_mul_f32_e32 v134, 0x3f317217, v132
	v_fma_f32 v134, v132, s52, -v134
	v_fmac_f32_e32 v134, 0x3377d1cf, v132
	v_fmac_f32_e32 v134, 0x3f317217, v132
	v_cmp_lt_f32_e64 s[0:1], |v132|, s53
	s_nop 1
	v_cndmask_b32_e64 v132, v132, v134, s[0:1]
	v_cndmask_b32_e32 v134, 0, v88, vcc
	v_sub_f32_e32 v132, v132, v134
	ds_read_b128 v[134:137], v13 offset:576
	ds_read_b128 v[138:141], v13 offset:592
	v_sub_f32_e32 v132, v133, v132
	v_fmamk_f32 v132, v132, 0x3d800000, v129
	s_waitcnt lgkmcnt(1)
	v_mov_b32_e32 v142, v134
	s_waitcnt lgkmcnt(0)
	v_mov_b32_e32 v143, v138
	v_mov_b32_e32 v138, v135
	v_pk_mul_f32 v[134:135], v[6:7], v[138:139]
	v_mov_b32_e32 v138, v136
	v_pk_fma_f32 v[134:135], v[2:3], v[142:143], v[134:135]
	v_mov_b32_e32 v139, v140
	v_pk_fma_f32 v[134:135], v[4:5], v[138:139], v[134:135]
	v_mov_b32_e32 v140, v137
	v_pk_fma_f32 v[134:135], v[58:59], v[140:141], v[134:135]
	s_nop 0
	v_add_f32_e32 v133, v121, v134
	v_add_f32_e32 v133, v133, v135
	ds_read_b128 v[134:137], v13 offset:608
	ds_read_b128 v[138:141], v13 offset:624
	s_waitcnt lgkmcnt(1)
	v_mov_b32_e32 v142, v134
	s_waitcnt lgkmcnt(0)
	v_mov_b32_e32 v143, v138
	v_mov_b32_e32 v138, v135
	v_pk_mul_f32 v[134:135], v[64:65], v[138:139]
	v_mov_b32_e32 v138, v136
	v_pk_fma_f32 v[134:135], v[60:61], v[142:143], v[134:135]
	v_mov_b32_e32 v139, v140
	v_pk_fma_f32 v[134:135], v[62:63], v[138:139], v[134:135]
	v_mov_b32_e32 v140, v137
	v_pk_fma_f32 v[134:135], v[66:67], v[140:141], v[134:135]
	s_nop 0
	v_add_f32_e32 v133, v133, v134
	v_add_f32_e32 v133, v133, v135
	v_min_f32_e32 v134, 0, v133
	v_mul_f32_e64 v133, |v133|, s50
	v_exp_f32_e32 v133, v133
	s_nop 0
	v_add_f32_e32 v133, 1.0, v133
	v_cmp_gt_f32_e32 vcc, s51, v133
	s_nop 1
	v_cndmask_b32_e64 v135, 0, 32, vcc
	v_ldexp_f32 v133, v133, v135
	v_log_f32_e32 v133, v133
	s_nop 0
	v_mul_f32_e32 v135, 0x3f317217, v133
	v_fma_f32 v135, v133, s52, -v135
	v_fmac_f32_e32 v135, 0x3377d1cf, v133
	v_fmac_f32_e32 v135, 0x3f317217, v133
	v_cmp_lt_f32_e64 s[0:1], |v133|, s53
	s_nop 1
	v_cndmask_b32_e64 v133, v133, v135, s[0:1]
	v_cndmask_b32_e32 v135, 0, v88, vcc
	v_sub_f32_e32 v133, v133, v135
	v_sub_f32_e32 v133, v134, v133
	ds_read_b128 v[134:137], v13 offset:640
	ds_read_b128 v[138:141], v13 offset:656
	v_fmamk_f32 v133, v133, 0x3d800000, v132
	s_waitcnt lgkmcnt(1)
	v_mov_b32_e32 v142, v134
	s_waitcnt lgkmcnt(0)
	v_mov_b32_e32 v143, v138
	v_mov_b32_e32 v138, v135
	v_pk_mul_f32 v[134:135], v[6:7], v[138:139]
	v_mov_b32_e32 v138, v136
	v_pk_fma_f32 v[134:135], v[2:3], v[142:143], v[134:135]
	v_mov_b32_e32 v139, v140
	v_pk_fma_f32 v[134:135], v[4:5], v[138:139], v[134:135]
	v_mov_b32_e32 v140, v137
	v_pk_fma_f32 v[134:135], v[58:59], v[140:141], v[134:135]
	s_nop 0
	v_add_f32_e32 v134, v121, v134
	v_add_f32_e32 v144, v134, v135
	ds_read_b128 v[134:137], v13 offset:672
	ds_read_b128 v[138:141], v13 offset:688
	s_waitcnt lgkmcnt(1)
	v_mov_b32_e32 v142, v134
	s_waitcnt lgkmcnt(0)
	v_mov_b32_e32 v143, v138
	v_mov_b32_e32 v138, v135
	v_pk_mul_f32 v[134:135], v[64:65], v[138:139]
	v_mov_b32_e32 v138, v136
	v_pk_fma_f32 v[134:135], v[60:61], v[142:143], v[134:135]
	v_mov_b32_e32 v139, v140
	v_pk_fma_f32 v[134:135], v[62:63], v[138:139], v[134:135]
	v_mov_b32_e32 v140, v137
	v_pk_fma_f32 v[134:135], v[66:67], v[140:141], v[134:135]
	s_nop 0
	v_add_f32_e32 v134, v144, v134
	v_add_f32_e32 v134, v134, v135
	v_min_f32_e32 v135, 0, v134
	v_mul_f32_e64 v134, |v134|, s50
	v_exp_f32_e32 v134, v134
	s_nop 0
	v_add_f32_e32 v134, 1.0, v134
	v_cmp_gt_f32_e32 vcc, s51, v134
	s_nop 1
	v_cndmask_b32_e64 v136, 0, 32, vcc
	v_ldexp_f32 v134, v134, v136
	v_log_f32_e32 v134, v134
	s_nop 0
	v_mul_f32_e32 v136, 0x3f317217, v134
	v_fma_f32 v136, v134, s52, -v136
	v_fmac_f32_e32 v136, 0x3377d1cf, v134
	v_fmac_f32_e32 v136, 0x3f317217, v134
	v_cmp_lt_f32_e64 s[0:1], |v134|, s53
	s_nop 1
	v_cndmask_b32_e64 v134, v134, v136, s[0:1]
	v_cndmask_b32_e32 v136, 0, v88, vcc
	v_sub_f32_e32 v134, v134, v136
	ds_read_b128 v[136:139], v13 offset:704
	ds_read_b128 v[140:143], v13 offset:720
	v_sub_f32_e32 v134, v135, v134
	v_fmamk_f32 v134, v134, 0x3d800000, v133
	s_waitcnt lgkmcnt(1)
	v_mov_b32_e32 v144, v136
	s_waitcnt lgkmcnt(0)
	v_mov_b32_e32 v145, v140
	v_mov_b32_e32 v140, v137
	v_pk_mul_f32 v[136:137], v[6:7], v[140:141]
	v_mov_b32_e32 v140, v138
	v_pk_fma_f32 v[136:137], v[2:3], v[144:145], v[136:137]
	v_mov_b32_e32 v141, v142
	v_pk_fma_f32 v[136:137], v[4:5], v[140:141], v[136:137]
	v_mov_b32_e32 v142, v139
	v_pk_fma_f32 v[136:137], v[58:59], v[142:143], v[136:137]
	s_nop 0
	v_add_f32_e32 v135, v121, v136
	v_add_f32_e32 v135, v135, v137
	ds_read_b128 v[136:139], v13 offset:736
	ds_read_b128 v[140:143], v13 offset:752
	s_waitcnt lgkmcnt(1)
	v_mov_b32_e32 v144, v136
	s_waitcnt lgkmcnt(0)
; #define LAS __attribute__((address_space(3)))
; __device__ __forceinline__ void gla_prep_unit(Frame& F, int unit) {
;     ...
;     for (int i = 0; i < 16; ++i) { const int c = cg * 16 + i; float z = bias;
; #pragma unroll
;         for (int r4 = 0; r4 < 4; ++r4) { const f32x4 g4 = *(const LAS f32x4*)(gaS + c * 16 + 4 * r4); z += g4.x * w2r[4 * r4] + g4.y * w2r[4 * r4 + 1] + g4.z * w2r[4 * r4 + 2] + g4.w * w2r[4 * r4 + 3]; }
;         const float ls = fminf(z, 0.f) - __logf(1.0f + __expf(-fabsf(z)));
;         run += ls * (1.f / 16.f); bl[i] = run; }
	v_mov_b32_e32 v145, v140
	v_mov_b32_e32 v140, v137
	v_pk_mul_f32 v[136:137], v[64:65], v[140:141]
	v_mov_b32_e32 v140, v138
	v_pk_fma_f32 v[136:137], v[60:61], v[144:145], v[136:137]
	v_mov_b32_e32 v141, v142
	v_pk_fma_f32 v[136:137], v[62:63], v[140:141], v[136:137]
	v_mov_b32_e32 v142, v139
	v_pk_fma_f32 v[136:137], v[66:67], v[142:143], v[136:137]
	s_nop 0
	v_add_f32_e32 v135, v135, v136
	v_add_f32_e32 v135, v135, v137
	v_min_f32_e32 v136, 0, v135
	v_mul_f32_e64 v135, |v135|, s50
	v_exp_f32_e32 v135, v135
	s_nop 0
	v_add_f32_e32 v135, 1.0, v135
	v_cmp_gt_f32_e32 vcc, s51, v135
	s_nop 1
	v_cndmask_b32_e64 v137, 0, 32, vcc
	v_ldexp_f32 v135, v135, v137
	v_log_f32_e32 v135, v135
	s_nop 0
	v_mul_f32_e32 v137, 0x3f317217, v135
	v_fma_f32 v137, v135, s52, -v137
	v_fmac_f32_e32 v137, 0x3377d1cf, v135
	v_fmac_f32_e32 v137, 0x3f317217, v135
	v_cmp_lt_f32_e64 s[0:1], |v135|, s53
	s_nop 1
	v_cndmask_b32_e64 v135, v135, v137, s[0:1]
	v_cndmask_b32_e32 v137, 0, v88, vcc
	v_sub_f32_e32 v135, v135, v137
	v_sub_f32_e32 v135, v136, v135
	ds_read_b128 v[136:139], v13 offset:768
	ds_read_b128 v[140:143], v13 offset:784
	v_fmamk_f32 v135, v135, 0x3d800000, v134
	s_waitcnt lgkmcnt(1)
	v_mov_b32_e32 v144, v136
	s_waitcnt lgkmcnt(0)
	v_mov_b32_e32 v145, v140
	v_mov_b32_e32 v140, v137
	v_pk_mul_f32 v[136:137], v[6:7], v[140:141]
	v_mov_b32_e32 v140, v138
	v_pk_fma_f32 v[136:137], v[2:3], v[144:145], v[136:137]
	v_mov_b32_e32 v141, v142
	v_pk_fma_f32 v[136:137], v[4:5], v[140:141], v[136:137]
	v_mov_b32_e32 v142, v139
	v_pk_fma_f32 v[136:137], v[58:59], v[142:143], v[136:137]
	s_nop 0
	v_add_f32_e32 v136, v121, v136
	v_add_f32_e32 v146, v136, v137
	ds_read_b128 v[136:139], v13 offset:800
	ds_read_b128 v[140:143], v13 offset:816
	s_waitcnt lgkmcnt(1)
	v_mov_b32_e32 v144, v136
	s_waitcnt lgkmcnt(0)
	v_mov_b32_e32 v145, v140
	v_mov_b32_e32 v140, v137
	v_pk_mul_f32 v[136:137], v[64:65], v[140:141]
	v_mov_b32_e32 v140, v138
	v_pk_fma_f32 v[136:137], v[60:61], v[144:145], v[136:137]
	v_mov_b32_e32 v141, v142
	v_pk_fma_f32 v[136:137], v[62:63], v[140:141], v[136:137]
	v_mov_b32_e32 v142, v139
	v_pk_fma_f32 v[136:137], v[66:67], v[142:143], v[136:137]
	s_nop 0
	v_add_f32_e32 v136, v146, v136
	v_add_f32_e32 v136, v136, v137
	v_min_f32_e32 v137, 0, v136
	v_mul_f32_e64 v136, |v136|, s50
	v_exp_f32_e32 v136, v136
	s_nop 0
	v_add_f32_e32 v136, 1.0, v136
	v_cmp_gt_f32_e32 vcc, s51, v136
	s_nop 1
	v_cndmask_b32_e64 v138, 0, 32, vcc
	v_ldexp_f32 v136, v136, v138
	v_log_f32_e32 v136, v136
	s_nop 0
	v_mul_f32_e32 v138, 0x3f317217, v136
	v_fma_f32 v138, v136, s52, -v138
	v_fmac_f32_e32 v138, 0x3377d1cf, v136
	v_fmac_f32_e32 v138, 0x3f317217, v136
	v_cmp_lt_f32_e64 s[0:1], |v136|, s53
	s_nop 1
	v_cndmask_b32_e64 v136, v136, v138, s[0:1]
	v_cndmask_b32_e32 v138, 0, v88, vcc
	v_sub_f32_e32 v136, v136, v138
	ds_read_b128 v[138:141], v13 offset:832
	ds_read_b128 v[142:145], v13 offset:848
	v_sub_f32_e32 v136, v137, v136
	v_fmamk_f32 v136, v136, 0x3d800000, v135
	s_waitcnt lgkmcnt(1)
	v_mov_b32_e32 v146, v138
	s_waitcnt lgkmcnt(0)
	v_mov_b32_e32 v147, v142
	v_mov_b32_e32 v142, v139
	v_pk_mul_f32 v[138:139], v[6:7], v[142:143]
	v_mov_b32_e32 v142, v140
	v_pk_fma_f32 v[138:139], v[2:3], v[146:147], v[138:139]
	v_mov_b32_e32 v143, v144
	v_pk_fma_f32 v[138:139], v[4:5], v[142:143], v[138:139]
	v_mov_b32_e32 v144, v141
	v_pk_fma_f32 v[138:139], v[58:59], v[144:145], v[138:139]
	s_nop 0
	v_add_f32_e32 v137, v121, v138
	v_add_f32_e32 v137, v137, v139
	ds_read_b128 v[138:141], v13 offset:864
	ds_read_b128 v[142:145], v13 offset:880
	s_waitcnt lgkmcnt(1)
	v_mov_b32_e32 v146, v138
	s_waitcnt lgkmcnt(0)
	v_mov_b32_e32 v147, v142
	v_mov_b32_e32 v142, v139
	v_pk_mul_f32 v[138:139], v[64:65], v[142:143]
	v_mov_b32_e32 v142, v140
	v_pk_fma_f32 v[138:139], v[60:61], v[146:147], v[138:139]
	v_mov_b32_e32 v143, v144
	v_pk_fma_f32 v[138:139], v[62:63], v[142:143], v[138:139]
	v_mov_b32_e32 v144, v141
	v_pk_fma_f32 v[138:139], v[66:67], v[144:145], v[138:139]
	s_nop 0
	v_add_f32_e32 v137, v137, v138
	v_add_f32_e32 v137, v137, v139
	v_min_f32_e32 v138, 0, v137
	v_mul_f32_e64 v137, |v137|, s50
	v_exp_f32_e32 v137, v137
	s_nop 0
	v_add_f32_e32 v137, 1.0, v137
	v_cmp_gt_f32_e32 vcc, s51, v137
	s_nop 1
	v_cndmask_b32_e64 v139, 0, 32, vcc
	v_ldexp_f32 v137, v137, v139
	v_log_f32_e32 v137, v137
	s_nop 0
	v_mul_f32_e32 v139, 0x3f317217, v137
	v_fma_f32 v139, v137, s52, -v139
	v_fmac_f32_e32 v139, 0x3377d1cf, v137
	v_fmac_f32_e32 v139, 0x3f317217, v137
	v_cmp_lt_f32_e64 s[0:1], |v137|, s53
	s_nop 1
	v_cndmask_b32_e64 v137, v137, v139, s[0:1]
	v_cndmask_b32_e32 v139, 0, v88, vcc
	v_sub_f32_e32 v137, v137, v139
	v_sub_f32_e32 v137, v138, v137
	ds_read_b128 v[138:141], v13 offset:896
	ds_read_b128 v[142:145], v13 offset:912
	v_fmamk_f32 v137, v137, 0x3d800000, v136
	s_waitcnt lgkmcnt(1)
	v_mov_b32_e32 v146, v138
	s_waitcnt lgkmcnt(0)
	v_mov_b32_e32 v147, v142
	v_mov_b32_e32 v142, v139
	v_pk_mul_f32 v[138:139], v[6:7], v[142:143]
	v_mov_b32_e32 v142, v140
	v_pk_fma_f32 v[138:139], v[2:3], v[146:147], v[138:139]
	v_mov_b32_e32 v143, v144
	v_pk_fma_f32 v[138:139], v[4:5], v[142:143], v[138:139]
	v_mov_b32_e32 v144, v141
	v_pk_fma_f32 v[138:139], v[58:59], v[144:145], v[138:139]
	s_nop 0
	v_add_f32_e32 v138, v121, v138
	v_add_f32_e32 v148, v138, v139
	ds_read_b128 v[138:141], v13 offset:928
	ds_read_b128 v[142:145], v13 offset:944
	s_waitcnt lgkmcnt(1)
	v_mov_b32_e32 v146, v138
	s_waitcnt lgkmcnt(0)
; #define LAS __attribute__((address_space(3)))
; __device__ __forceinline__ unsigned f2bf(float f) { unsigned u = __builtin_bit_cast(unsigned, f); return (u + 0x7fffu + ((u >> 16) & 1u)) >> 16; }
; __device__ __forceinline__ void gla_prep_unit(Frame& F, int unit) {
;     ...
;     for (int i = 0; i < 16; ++i) { const int c = cg * 16 + i; float z = bias;
; #pragma unroll
;         for (int r4 = 0; r4 < 4; ++r4) { const f32x4 g4 = *(const LAS f32x4*)(gaS + c * 16 + 4 * r4); z += g4.x * w2r[4 * r4] + g4.y * w2r[4 * r4 + 1] + g4.z * w2r[4 * r4 + 2] + g4.w * w2r[4 * r4 + 3]; }
;         const float ls = fminf(z, 0.f) - __logf(1.0f + __expf(-fabsf(z)));
;         run += ls * (1.f / 16.f); bl[i] = run; }
;     tot[cg * 128 + d] = run;
;     __syncthreads();
;     float offs = 0.f, blast = 0.f;
; #pragma unroll
;     for (int g = 0; g < 4; ++g) { const float t = tot[g * 128 + d]; blast += t; if (g < cg) offs += t; }
;     const float eblast = __expf(blast);
;     unsigned kd[8];
; #pragma unroll
;     for (int i = 0; i < 16; i += 2) { float kdv[2];
; #pragma unroll
;         for (int u = 0; u < 2; ++u) { const int c = cg * 16 + i + u; const float bb = bl[i + u] + offs;
;             const float q = bf2f(qv[i + u]) * 0.08838834764831845f, k = bf2f(kv[i + u]);
;             const float eb = __expf(bb), einv = __builtin_amdgcn_rcpf(eb);
;             const float qin = q * eb, kin = k * einv; kdv[u] = kin * eblast;
;             const bf16_t qb16 = (bf16_t)f2bf(qin); qinS[c * GP_ROW + d] = qb16; kinS[c * GP_ROW + d] = (bf16_t)f2bf(kin); QIN[c * 128 + d] = qb16; }
	v_mov_b32_e32 v147, v142
	v_mov_b32_e32 v142, v139
	v_pk_mul_f32 v[138:139], v[64:65], v[142:143]
	v_mov_b32_e32 v142, v140
	v_pk_fma_f32 v[138:139], v[60:61], v[146:147], v[138:139]
	v_mov_b32_e32 v143, v144
	v_pk_fma_f32 v[138:139], v[62:63], v[142:143], v[138:139]
	v_mov_b32_e32 v144, v141
	v_pk_fma_f32 v[138:139], v[66:67], v[144:145], v[138:139]
	s_nop 0
	v_add_f32_e32 v138, v148, v138
	v_add_f32_e32 v138, v138, v139
	v_min_f32_e32 v139, 0, v138
	v_mul_f32_e64 v138, |v138|, s50
	v_exp_f32_e32 v138, v138
	s_nop 0
	v_add_f32_e32 v138, 1.0, v138
	v_cmp_gt_f32_e32 vcc, s51, v138
	s_nop 1
	v_cndmask_b32_e64 v140, 0, 32, vcc
	v_ldexp_f32 v138, v138, v140
	v_log_f32_e32 v138, v138
	s_nop 0
	v_mul_f32_e32 v140, 0x3f317217, v138
	v_fma_f32 v140, v138, s52, -v140
	v_fmac_f32_e32 v140, 0x3377d1cf, v138
	v_fmac_f32_e32 v140, 0x3f317217, v138
	v_cmp_lt_f32_e64 s[0:1], |v138|, s53
	s_nop 1
	v_cndmask_b32_e64 v138, v138, v140, s[0:1]
	v_cndmask_b32_e32 v140, 0, v88, vcc
	v_sub_f32_e32 v138, v138, v140
	ds_read_b128 v[140:143], v13 offset:960
	ds_read_b128 v[144:147], v13 offset:976
	v_sub_f32_e32 v138, v139, v138
	v_fmamk_f32 v138, v138, 0x3d800000, v137
	s_waitcnt lgkmcnt(1)
	v_mov_b32_e32 v148, v140
	s_waitcnt lgkmcnt(0)
	v_mov_b32_e32 v149, v144
	v_mov_b32_e32 v144, v141
	v_pk_mul_f32 v[6:7], v[6:7], v[144:145]
	s_nop 0
	v_pk_fma_f32 v[2:3], v[2:3], v[148:149], v[6:7]
	v_mov_b32_e32 v6, v142
	v_mov_b32_e32 v7, v146
	v_pk_fma_f32 v[2:3], v[4:5], v[6:7], v[2:3]
	v_mov_b32_e32 v146, v143
	v_pk_fma_f32 v[2:3], v[58:59], v[146:147], v[2:3]
	s_nop 0
	v_add_f32_e32 v2, v121, v2
	v_add_f32_e32 v58, v2, v3
	ds_read_b128 v[2:5], v13 offset:992
	ds_read_b128 v[140:143], v13 offset:1008
	s_waitcnt lgkmcnt(1)
	v_mov_b32_e32 v6, v2
	s_waitcnt lgkmcnt(0)
	v_mov_b32_e32 v7, v140
	v_mov_b32_e32 v140, v3
	v_pk_mul_f32 v[2:3], v[64:65], v[140:141]
	s_nop 0
	v_pk_fma_f32 v[2:3], v[60:61], v[6:7], v[2:3]
	v_mov_b32_e32 v6, v4
	v_mov_b32_e32 v7, v142
	v_pk_fma_f32 v[2:3], v[62:63], v[6:7], v[2:3]
	v_mov_b32_e32 v142, v5
	v_pk_fma_f32 v[2:3], v[66:67], v[142:143], v[2:3]
	s_nop 0
	v_add_f32_e32 v2, v58, v2
	v_add_f32_e32 v2, v2, v3
	v_min_f32_e32 v3, 0, v2
	v_mul_f32_e64 v2, |v2|, s50
	v_exp_f32_e32 v2, v2
	v_lshl_add_u64 v[58:59], s[66:67], 0, v[28:29]
	v_add_f32_e32 v2, 1.0, v2
	v_cmp_gt_f32_e32 vcc, s51, v2
	s_nop 1
	v_cndmask_b32_e64 v4, 0, 32, vcc
	v_ldexp_f32 v2, v2, v4
	v_log_f32_e32 v2, v2
	s_nop 0
	v_mul_f32_e32 v4, 0x3f317217, v2
	v_fma_f32 v4, v2, s52, -v4
	v_fmac_f32_e32 v4, 0x3377d1cf, v2
	v_fmac_f32_e32 v4, 0x3f317217, v2
	v_cmp_lt_f32_e64 s[0:1], |v2|, s53
	s_nop 1
	v_cndmask_b32_e64 v2, v2, v4, s[0:1]
	v_cndmask_b32_e32 v4, 0, v88, vcc
	v_sub_f32_e32 v2, v2, v4
	v_sub_f32_e32 v2, v3, v2
	v_fmamk_f32 v3, v2, 0x3d800000, v138
	ds_write_b32 v68, v3 offset:4096
	s_waitcnt lgkmcnt(0)
	s_barrier
	ds_read2st64_b32 v[4:5], v69 offset0:16 offset1:18
	s_waitcnt lgkmcnt(0)
	v_add_f32_e32 v2, 0, v4
	v_cndmask_b32_e64 v4, v2, 0, s[4:5]
	v_add_f32_e32 v2, v2, v5
	v_add_f32_e32 v5, v5, v4
	v_cndmask_b32_e64 v6, v4, v5, s[6:7]
	ds_read2st64_b32 v[4:5], v69 offset0:20 offset1:22
	s_waitcnt lgkmcnt(0)
	v_add_f32_e32 v2, v2, v4
	v_add_f32_e32 v4, v4, v6
	v_cndmask_b32_e64 v4, v6, v4, s[8:9]
	v_add_f32_e32 v2, v2, v5
	v_add_f32_e32 v5, v5, v4
	v_cndmask_b32_e64 v62, v4, v5, s[10:11]
	v_add_f32_e32 v4, v122, v62
	v_mul_f32_e32 v4, 0x3fb8aa3b, v4
	v_exp_f32_e32 v6, v4
	v_lshlrev_b32_e32 v5, 16, v120
	v_mul_f32_e32 v5, 0x3db504f3, v5
	v_mul_f32_e32 v2, 0x3fb8aa3b, v2
	v_mul_f32_e32 v5, v5, v6
	v_rcp_f32_e32 v4, v6
	v_bfe_u32 v6, v5, 16, 1
	v_add3_u32 v5, v5, v6, s55
	v_lshrrev_b32_e32 v5, 16, v5
	v_lshl_add_u64 v[6:7], s[66:67], 0, v[26:27]
	ds_write_b16 v70, v5 offset:8192
	global_store_short v[6:7], v5, off
	v_add_f32_e32 v5, v123, v62
	v_mul_f32_e32 v5, 0x3fb8aa3b, v5
	v_exp_f32_e32 v5, v5
	v_lshlrev_b32_e32 v6, 16, v119
	v_mul_f32_e32 v7, 0x3db504f3, v6
	v_exp_f32_e32 v2, v2
	v_rcp_f32_e32 v6, v5
	v_mul_f32_e32 v5, v7, v5
	v_bfe_u32 v7, v5, 16, 1
	v_add3_u32 v5, v5, v7, s55
	v_lshrrev_b32_e32 v60, 16, v5
	v_add_f32_e32 v5, v124, v62
	v_mul_f32_e32 v5, 0x3fb8aa3b, v5
	global_store_short v[58:59], v60, off
	v_exp_f32_e32 v58, v5
	v_lshlrev_b32_e32 v7, 16, v117
	v_mul_f32_e32 v7, 0x3db504f3, v7
	v_mul_f32_e32 v7, v7, v58
	v_rcp_f32_e32 v5, v58
	v_bfe_u32 v58, v7, 16, 1
	v_add3_u32 v7, v7, v58, s55
	v_lshrrev_b32_e32 v63, 16, v7
	v_add_f32_e32 v7, v125, v62
	v_lshl_add_u64 v[58:59], s[66:67], 0, v[30:31]
	v_mul_f32_e32 v7, 0x3fb8aa3b, v7
	global_store_short v[58:59], v63, off
	v_exp_f32_e32 v59, v7
	v_lshlrev_b32_e32 v58, 16, v118
	v_mul_f32_e32 v58, 0x3db504f3, v58
	v_mul_f32_e32 v58, v58, v59
	v_rcp_f32_e32 v7, v59
	v_bfe_u32 v59, v58, 16, 1
	v_add3_u32 v58, v58, v59, s55
	v_lshrrev_b32_e32 v64, 16, v58
	v_lshl_add_u64 v[58:59], s[66:67], 0, v[32:33]
	global_store_short v[58:59], v64, off
	v_lshlrev_b32_e32 v59, 16, v114
	v_lshlrev_b32_e32 v58, 16, v115
	v_pk_mul_f32 v[58:59], v[4:5], v[58:59]
	v_lshlrev_b32_e32 v5, 16, v112
	v_bfe_u32 v4, v58, 16, 1
	v_add3_u32 v4, v58, v4, s55
	ds_write_b16_d16_hi v70, v4 offset:25600
	ds_write_b16 v71, v60 offset:8192
	v_lshlrev_b32_e32 v4, 16, v111
	v_pk_mul_f32 v[60:61], v[6:7], v[4:5]
	v_bfe_u32 v6, v59, 16, 1
	v_bfe_u32 v4, v60, 16, 1
	v_add3_u32 v4, v60, v4, s55
	ds_write_b16_d16_hi v71, v4 offset:25600
	v_pk_mul_f32 v[4:5], v[2:3], v[58:59] op_sel_hi:[0,1]
	v_bfe_u32 v58, v61, 16, 1
	v_add3_u32 v58, v61, v58, s55
	ds_write_b16 v72, v63 offset:8192
	ds_write_b16_d16_hi v73, v58 offset:25600
	v_add_f32_e32 v58, v126, v62
	v_add3_u32 v6, v59, v6, s55
	v_mul_f32_e32 v58, 0x3fb8aa3b, v58
	ds_write_b16_d16_hi v72, v6 offset:25600
; __device__ __forceinline__ unsigned f2bf(float f) { unsigned u = __builtin_bit_cast(unsigned, f); return (u + 0x7fffu + ((u >> 16) & 1u)) >> 16; }
; __device__ __forceinline__ unsigned pk2(float lo, float hi) { return f2bf(lo) | (f2bf(hi) << 16); }
; __device__ __forceinline__ void gla_prep_unit(Frame& F, int unit) {
;     ...
;     for (int i = 0; i < 16; i += 2) { float kdv[2];
; #pragma unroll
;         for (int u = 0; u < 2; ++u) { const int c = cg * 16 + i + u; const float bb = bl[i + u] + offs;
;             const float q = bf2f(qv[i + u]) * 0.08838834764831845f, k = bf2f(kv[i + u]);
;             const float eb = __expf(bb), einv = __builtin_amdgcn_rcpf(eb);
;             const float qin = q * eb, kin = k * einv; kdv[u] = kin * eblast;
;             const bf16_t qb16 = (bf16_t)f2bf(qin); qinS[c * GP_ROW + d] = qb16; kinS[c * GP_ROW + d] = (bf16_t)f2bf(kin); QIN[c * 128 + d] = qb16; }
;         kd[i >> 1] = pk2(kdv[0], kdv[1]); }
	v_pk_mul_f32 v[6:7], v[2:3], v[60:61] op_sel_hi:[0,1]
	v_exp_f32_e32 v60, v58
	v_lshlrev_b32_e32 v59, 16, v110
	v_mul_f32_e32 v59, 0x3db504f3, v59
	ds_write_b16 v73, v64 offset:8192
	v_mul_f32_e32 v59, v59, v60
	v_rcp_f32_e32 v58, v60
	v_bfe_u32 v60, v59, 16, 1
	v_add3_u32 v59, v59, v60, s55
	v_lshrrev_b32_e32 v59, 16, v59
	v_lshl_add_u64 v[60:61], s[66:67], 0, v[34:35]
	ds_write_b16 v74, v59 offset:8192
	global_store_short v[60:61], v59, off
	v_add_f32_e32 v59, v127, v62
	v_mul_f32_e32 v59, 0x3fb8aa3b, v59
	v_exp_f32_e32 v59, v59
	v_lshlrev_b32_e32 v60, 16, v109
	v_mul_f32_e32 v61, 0x3db504f3, v60
	v_lshl_add_u64 v[64:65], s[66:67], 0, v[36:37]
	v_rcp_f32_e32 v60, v59
	v_mul_f32_e32 v59, v61, v59
	v_bfe_u32 v61, v59, 16, 1
	v_add3_u32 v59, v59, v61, s55
	v_lshrrev_b32_e32 v63, 16, v59
	v_add_f32_e32 v59, v128, v62
	v_mul_f32_e32 v59, 0x3fb8aa3b, v59
	global_store_short v[64:65], v63, off
	v_exp_f32_e32 v64, v59
	v_lshlrev_b32_e32 v61, 16, v107
	v_mul_f32_e32 v61, 0x3db504f3, v61
	v_mul_f32_e32 v61, v61, v64
	v_rcp_f32_e32 v59, v64
	v_bfe_u32 v64, v61, 16, 1
	v_add3_u32 v61, v61, v64, s55
	v_lshrrev_b32_e32 v107, 16, v61
	v_add_f32_e32 v61, v129, v62
	v_lshl_add_u64 v[64:65], s[66:67], 0, v[38:39]
	v_mul_f32_e32 v61, 0x3fb8aa3b, v61
	global_store_short v[64:65], v107, off
	v_exp_f32_e32 v65, v61
	v_lshlrev_b32_e32 v64, 16, v104
	v_mul_f32_e32 v64, 0x3db504f3, v64
	v_mul_f32_e32 v64, v64, v65
	v_rcp_f32_e32 v61, v65
	v_bfe_u32 v65, v64, 16, 1
	v_add3_u32 v64, v64, v65, s55
	v_lshrrev_b32_e32 v104, 16, v64
	v_lshl_add_u64 v[64:65], s[66:67], 0, v[40:41]
	global_store_short v[64:65], v104, off
	v_lshlrev_b32_e32 v65, 16, v101
	v_lshlrev_b32_e32 v64, 16, v100
	v_pk_mul_f32 v[64:65], v[58:59], v[64:65]
	v_lshlrev_b32_e32 v59, 16, v105
	v_bfe_u32 v58, v64, 16, 1
	v_add3_u32 v58, v64, v58, s55
	ds_write_b16_d16_hi v74, v58 offset:25600
	ds_write_b16 v75, v63 offset:8192
	v_lshlrev_b32_e32 v58, 16, v102
	v_pk_mul_f32 v[66:67], v[60:61], v[58:59]
	v_bfe_u32 v60, v65, 16, 1
	v_bfe_u32 v58, v66, 16, 1
	v_bfe_u32 v63, v67, 16, 1
	v_add3_u32 v58, v66, v58, s55
	v_add3_u32 v60, v65, v60, s55
	v_add3_u32 v63, v67, v63, s55
	ds_write_b16_d16_hi v75, v58 offset:25600
	ds_write_b16 v76, v107 offset:8192
	ds_write_b16_d16_hi v76, v60 offset:25600
	ds_write_b16_d16_hi v77, v63 offset:25600
	v_add_f32_e32 v63, v132, v62
	v_mul_f32_e32 v63, 0x3fb8aa3b, v63
	v_exp_f32_e32 v63, v63
	v_pk_mul_f32 v[58:59], v[2:3], v[64:65] op_sel_hi:[0,1]
	v_lshlrev_b32_e32 v64, 16, v116
	v_mul_f32_e32 v65, 0x3db504f3, v64
	v_rcp_f32_e32 v64, v63
	v_mul_f32_e32 v63, v65, v63
	v_bfe_u32 v65, v63, 16, 1
	v_add3_u32 v63, v63, v65, s55
	v_pk_mul_f32 v[60:61], v[2:3], v[66:67] op_sel_hi:[0,1]
	v_lshrrev_b32_e32 v63, 16, v63
	v_lshl_add_u64 v[66:67], s[66:67], 0, v[42:43]
	ds_write_b16 v77, v104 offset:8192
	ds_write_b16 v78, v63 offset:8192
	global_store_short v[66:67], v63, off
	v_add_f32_e32 v63, v133, v62
	v_mul_f32_e32 v63, 0x3fb8aa3b, v63
	v_exp_f32_e32 v63, v63
	v_lshlrev_b32_e32 v65, 16, v113
	v_mul_f32_e32 v65, 0x3db504f3, v65
	v_lshl_add_u64 v[100:101], s[66:67], 0, v[44:45]
	v_rcp_f32_e32 v66, v63
	v_mul_f32_e32 v63, v65, v63
	v_bfe_u32 v65, v63, 16, 1
	v_add3_u32 v63, v63, v65, s55
	v_add_f32_e32 v65, v134, v62
	v_lshrrev_b32_e32 v63, 16, v63
	v_mul_f32_e32 v65, 0x3fb8aa3b, v65
	global_store_short v[100:101], v63, off
	v_exp_f32_e32 v100, v65
	v_lshlrev_b32_e32 v67, 16, v108
	v_mul_f32_e32 v67, 0x3db504f3, v67
	v_mul_f32_e32 v67, v67, v100
	v_rcp_f32_e32 v65, v100
	v_bfe_u32 v100, v67, 16, 1
	v_add3_u32 v67, v67, v100, s55
	v_lshrrev_b32_e32 v102, 16, v67
	v_add_f32_e32 v67, v135, v62
	v_lshl_add_u64 v[100:101], s[66:67], 0, v[46:47]
	v_mul_f32_e32 v67, 0x3fb8aa3b, v67
	global_store_short v[100:101], v102, off
	v_exp_f32_e32 v101, v67
	v_lshlrev_b32_e32 v100, 16, v106
	v_mul_f32_e32 v100, 0x3db504f3, v100
	v_mul_f32_e32 v100, v100, v101
	v_rcp_f32_e32 v67, v101
	v_bfe_u32 v101, v100, 16, 1
	v_add3_u32 v100, v100, v101, s55
	v_lshrrev_b32_e32 v104, 16, v100
	v_lshl_add_u64 v[100:101], s[66:67], 0, v[48:49]
	global_store_short v[100:101], v104, off
	v_lshlrev_b32_e32 v101, 16, v103
	v_lshlrev_b32_e32 v100, 16, v99
	v_pk_mul_f32 v[64:65], v[64:65], v[100:101]
	v_lshl_add_u64 v[100:101], s[66:67], 0, v[52:53]
	v_bfe_u32 v99, v64, 16, 1
	v_add3_u32 v99, v64, v99, s55
	ds_write_b16_d16_hi v78, v99 offset:25600
	ds_write_b16 v79, v63 offset:8192
	v_lshlrev_b32_e32 v99, 16, v98
	v_lshlrev_b32_e32 v98, 16, v97
	v_pk_mul_f32 v[66:67], v[66:67], v[98:99]
	v_pk_mul_f32 v[98:99], v[2:3], v[64:65] op_sel_hi:[0,1]
	v_bfe_u32 v63, v66, 16, 1
	v_add3_u32 v63, v66, v63, s55
	ds_write_b16_d16_hi v79, v63 offset:25600
	v_bfe_u32 v63, v65, 16, 1
; __device__ __forceinline__ unsigned f2bf(float f) { unsigned u = __builtin_bit_cast(unsigned, f); return (u + 0x7fffu + ((u >> 16) & 1u)) >> 16; }
; __device__ __forceinline__ unsigned pk2(float lo, float hi) { return f2bf(lo) | (f2bf(hi) << 16); }
; __device__ __forceinline__ void gla_prep_unit(Frame& F, int unit) {
;     ...
;     for (int i = 0; i < 16; i += 2) { float kdv[2];
; #pragma unroll
;         for (int u = 0; u < 2; ++u) { const int c = cg * 16 + i + u; const float bb = bl[i + u] + offs;
;             const float q = bf2f(qv[i + u]) * 0.08838834764831845f, k = bf2f(kv[i + u]);
;             const float eb = __expf(bb), einv = __builtin_amdgcn_rcpf(eb);
;             const float qin = q * eb, kin = k * einv; kdv[u] = kin * eblast;
;             const bf16_t qb16 = (bf16_t)f2bf(qin); qinS[c * GP_ROW + d] = qb16; kinS[c * GP_ROW + d] = (bf16_t)f2bf(kin); QIN[c * 128 + d] = qb16; }
;         kd[i >> 1] = pk2(kdv[0], kdv[1]); }
;     *(u32x4*)(KDT + d * 64 + cg * 16) = (u32x4){kd[0], kd[1], kd[2], kd[3]}; *(u32x4*)(KDT + d * 64 + cg * 16 + 8) = (u32x4){kd[4], kd[5], kd[6], kd[7]};
;     if (cg == 0) DEC[d] = eblast;
	v_add3_u32 v63, v65, v63, s55
	ds_write_b16_d16_hi v80, v63 offset:25600
	v_bfe_u32 v63, v67, 16, 1
	v_add3_u32 v63, v67, v63, s55
	ds_write_b16 v80, v102 offset:8192
	ds_write_b16_d16_hi v81, v63 offset:25600
	v_add_f32_e32 v63, v136, v62
	v_mul_f32_e32 v63, 0x3fb8aa3b, v63
	v_exp_f32_e32 v63, v63
	v_pk_mul_f32 v[64:65], v[2:3], v[66:67] op_sel_hi:[0,1]
	v_lshlrev_b32_e32 v66, 16, v96
	v_mul_f32_e32 v67, 0x3db504f3, v66
	v_rcp_f32_e32 v66, v63
	v_mul_f32_e32 v63, v67, v63
	v_bfe_u32 v67, v63, 16, 1
	v_add3_u32 v63, v63, v67, s55
	v_lshrrev_b32_e32 v63, 16, v63
	v_lshl_add_u64 v[96:97], s[66:67], 0, v[50:51]
	ds_write_b16 v81, v104 offset:8192
	ds_write_b16 v82, v63 offset:8192
	global_store_short v[96:97], v63, off
	v_add_f32_e32 v63, v137, v62
	v_mul_f32_e32 v63, 0x3fb8aa3b, v63
	v_exp_f32_e32 v63, v63
	v_lshlrev_b32_e32 v67, 16, v95
	v_mul_f32_e32 v67, 0x3db504f3, v67
	v_add_f32_e32 v3, v62, v3
	v_rcp_f32_e32 v96, v63
	v_mul_f32_e32 v63, v67, v63
	v_bfe_u32 v67, v63, 16, 1
	v_add3_u32 v63, v63, v67, s55
	v_lshrrev_b32_e32 v102, 16, v63
	v_add_f32_e32 v63, v138, v62
	v_mul_f32_e32 v63, 0x3fb8aa3b, v63
	v_mul_f32_e32 v3, 0x3fb8aa3b, v3
	v_exp_f32_e32 v63, v63
	v_exp_f32_e32 v3, v3
	v_lshlrev_b32_e32 v67, 16, v94
	v_lshlrev_b32_e32 v62, 16, v93
	v_mul_f32_e32 v94, 0x3db504f3, v67
	v_mul_f32_e32 v62, 0x3db504f3, v62
	v_rcp_f32_e32 v67, v63
	v_mul_f32_e32 v63, v94, v63
	v_rcp_f32_e32 v97, v3
	v_mul_f32_e32 v3, v62, v3
	v_bfe_u32 v94, v63, 16, 1
	v_bfe_u32 v62, v3, 16, 1
	v_add3_u32 v63, v63, v94, s55
	v_add3_u32 v3, v3, v62, s55
	global_store_short v[100:101], v102, off
	v_lshrrev_b32_e32 v100, 16, v63
	v_lshl_add_u64 v[94:95], s[66:67], 0, v[54:55]
	v_lshrrev_b32_e32 v3, 16, v3
	v_lshl_add_u64 v[62:63], s[66:67], 0, v[56:57]
	global_store_short v[94:95], v100, off
	global_store_short v[62:63], v3, off
	v_lshlrev_b32_e32 v63, 16, v92
	v_lshlrev_b32_e32 v62, 16, v91
	v_pk_mul_f32 v[62:63], v[66:67], v[62:63]
	v_lshlrev_b32_e32 v67, 16, v90
	v_bfe_u32 v66, v62, 16, 1
	v_add3_u32 v66, v62, v66, s55
	ds_write_b16_d16_hi v82, v66 offset:25600
	ds_write_b16 v83, v102 offset:8192
	v_lshlrev_b32_e32 v66, 16, v89
	v_pk_mul_f32 v[66:67], v[96:97], v[66:67]
	v_pk_mul_f32 v[90:91], v[2:3], v[62:63] op_sel_hi:[0,1]
	v_bfe_u32 v89, v66, 16, 1
	v_bfe_u32 v62, v63, 16, 1
	v_add3_u32 v89, v66, v89, s55
	v_add3_u32 v62, v63, v62, s55
	ds_write_b16_d16_hi v83, v89 offset:25600
	ds_write_b16 v84, v100 offset:8192
	ds_write_b16_d16_hi v84, v62 offset:25600
	v_pk_mul_f32 v[62:63], v[2:3], v[66:67] op_sel_hi:[0,1]
	ds_write_b16 v85, v3 offset:8192
	v_bfe_u32 v3, v67, 16, 1
	v_add3_u32 v3, v67, v3, s55
	v_bfe_u32 v67, v7, 16, 1
	v_bfe_u32 v66, v60, 16, 1
	v_bfe_u32 v89, v6, 16, 1
	v_add3_u32 v67, v7, v67, s55
	v_bfe_u32 v7, v58, 16, 1
	ds_write_b16_d16_hi v85, v3 offset:25600
	v_bfe_u32 v3, v61, 16, 1
	v_add3_u32 v89, v6, v89, s55
	v_add3_u32 v6, v60, v66, s55
	v_bfe_u32 v60, v59, 16, 1
	v_add3_u32 v7, v58, v7, s55
	v_add3_u32 v3, v61, v3, s55
	v_bfe_u32 v61, v4, 16, 1
	v_bfe_u32 v66, v5, 16, 1
	v_add3_u32 v59, v59, v60, s55
	v_lshrrev_b32_e32 v58, 16, v7
	v_add3_u32 v5, v5, v66, s55
	v_add3_u32 v4, v4, v61, s55
	v_lshrrev_b32_e32 v7, 16, v59
	v_and_or_b32 v6, v6, s45, v58
	v_lshl_add_u64 v[58:59], s[66:67], 0, v[24:25]
	v_lshrrev_b32_e32 v4, 16, v4
	v_lshrrev_b32_e32 v5, 16, v5
	v_add_co_u32_e32 v58, vcc, s56, v58
	v_and_or_b32 v7, v3, s45, v7
	v_and_or_b32 v5, v67, s45, v5
	v_and_or_b32 v4, v89, s45, v4
	v_addc_co_u32_e32 v59, vcc, 0, v59, vcc
	global_store_dwordx4 v[58:59], v[4:7], off
	v_bfe_u32 v61, v90, 16, 1
	v_bfe_u32 v3, v63, 16, 1
	v_bfe_u32 v4, v62, 16, 1
	v_bfe_u32 v6, v64, 16, 1
	v_add3_u32 v60, v64, v6, s55
	v_add3_u32 v4, v62, v4, s55
	v_bfe_u32 v6, v98, 16, 1
	v_bfe_u32 v7, v99, 16, 1
	v_bfe_u32 v62, v91, 16, 1
	v_bfe_u32 v5, v65, 16, 1
	v_add3_u32 v62, v91, v62, s55
	v_add3_u32 v61, v90, v61, s55
	v_add3_u32 v7, v99, v7, s55
	v_add3_u32 v6, v98, v6, s55
	v_add3_u32 v5, v65, v5, s55
	v_add3_u32 v3, v63, v3, s55
	v_lshrrev_b32_e32 v63, 16, v6
	v_lshrrev_b32_e32 v64, 16, v7
	v_lshrrev_b32_e32 v6, 16, v61
	v_lshrrev_b32_e32 v7, 16, v62
	v_and_or_b32 v7, v3, s45, v7
	v_and_or_b32 v6, v4, s45, v6
	v_and_or_b32 v5, v5, s45, v64
	v_and_or_b32 v4, v60, s45, v63
	global_store_dwordx4 v[58:59], v[4:7], off offset:16
	s_and_saveexec_b64 s[0:1], s[4:5]
	s_cbranch_execz .LBB0_266
	v_readlane_b32 s60, v254, 25
	v_readlane_b32 s66, v254, 31
	v_readlane_b32 s67, v254, 32
	v_readlane_b32 s61, v254, 26
	v_readlane_b32 s62, v254, 27
	v_lshl_add_u64 v[4:5], s[66:67], 0, v[18:19]
	v_readlane_b32 s63, v254, 28
	v_readlane_b32 s64, v254, 29
	v_readlane_b32 s65, v254, 30
	global_store_dword v[4:5], v2, off
